# FFN-up layer-0 conversion slots take two items per wave (2048 more items out of the prologue, which keeps 6656)
# speedup vs baseline: 1.0041x; 1.0041x over previous
.LBB0_947:
	s_or_b64 exec, exec, s[30:31]
	v_mov_b32_e32 v6, v0
	s_mov_b64 s[0:1], 0
	v_readlane_b32 s36, v253, 8
	s_waitcnt lgkmcnt(0)
	s_barrier
	v_readlane_b32 s1, v253, 9
	s_cmpk_lg_i32 s1, 0x100
	s_cbranch_scc1 .Lfs1_skip
	v_readlane_b32 s1, v254, 20
	s_cmp_eq_u32 s1, 0
	s_cbranch_scc1 .Lfs1_skip
	s_cmpk_gt_i32 s36, 0x7f
	s_cbranch_scc1 .Lfs1_skip
	v_readfirstlane_b32 s1, v0
	s_lshl_b32 s0, s36, 3
	s_lshr_b32 s1, s1, 6
	s_add_i32 s0, s0, s1
	s_addk_i32 s0, 0x2e00
	s_mov_b32 s101, 1
	s_mov_b32 s100, 0
	v_readlane_b32 s62, v253, 54
	v_readlane_b32 s26, v253, 55
	s_mov_b32 s73, 0x10000
	v_mov_b32_e32 v135, v0
	v_and_b32_e32 v132, 63, v0
	s_branch .Ltkf_go
.Lfret_1:
	s_cmp_lg_u32 s100, 0
	s_cbranch_scc1 .Lfret_1b
	s_mov_b32 s100, 1
	v_readfirstlane_b32 s1, v0
	s_lshl_b32 s0, s36, 3
	s_lshr_b32 s1, s1, 6
	s_add_i32 s0, s0, s1
	s_addk_i32 s0, 0x1e00
	v_readlane_b32 s62, v253, 54
	v_readlane_b32 s26, v253, 55
	s_mov_b32 s73, 0x10000
	v_mov_b32_e32 v135, v0
	v_and_b32_e32 v132, 63, v0
	s_branch .Ltkf_go

.LBB0_971:
	s_waitcnt vmcnt(0)
	s_barrier
	v_readlane_b32 s1, v253, 9
	s_cmpk_lg_i32 s1, 0x100
	s_cbranch_scc1 .Lfs2_skip
	v_readlane_b32 s1, v254, 20
	s_cmp_eq_u32 s1, 0
	s_cbranch_scc1 .Lfs2_skip
	v_readlane_b32 s27, v253, 8
	s_cmpk_lt_i32 s27, 0x80
	s_cbranch_scc1 .Lfs2_skip
	v_readfirstlane_b32 s1, v0
	s_lshl_b32 s0, s27, 3
	s_lshr_b32 s1, s1, 6
	s_add_i32 s0, s0, s1
	s_addk_i32 s0, 0x2600
	s_mov_b32 s101, 2
	s_mov_b32 s100, 0
	v_readlane_b32 s62, v253, 54
	v_readlane_b32 s26, v253, 55
	s_mov_b32 s73, 0x10000
	v_mov_b32_e32 v135, v0
	v_and_b32_e32 v132, 63, v0
	s_branch .Ltkf_go
.Lfret_2:
	s_cmp_lg_u32 s100, 0
	s_cbranch_scc1 .Lfret_2b
	s_mov_b32 s100, 1
	v_readlane_b32 s27, v253, 8
	v_readfirstlane_b32 s1, v0
	s_lshl_b32 s0, s27, 3
	s_lshr_b32 s1, s1, 6
	s_add_i32 s0, s0, s1
	s_addk_i32 s0, 0x1600
	v_readlane_b32 s62, v253, 54
	v_readlane_b32 s26, v253, 55
	s_mov_b32 s73, 0x10000
	v_mov_b32_e32 v135, v0
	v_and_b32_e32 v132, 63, v0
	s_branch .Ltkf_go
